# instruction selection in ml_out epilogue: f32->bf16 bit trick (bfe/add3/lshr/and_or) replaced by v_cvt_pk_bf16_f32 (same RNE): staging pairs + output packs, ~290 fewer VALU per pass; on top of v52
# speedup vs baseline: 1.0224x; 1.0043x over previous
.LBB0_742:
	s_or_b64 exec, exec, s[80:81]
	ds_bpermute_b32 v41, v241, v120
	ds_bpermute_b32 v40, v241, v119
	ds_bpermute_b32 v7, v241, v118
	v_mov_b32_e32 v42, v114
	v_mov_b32_e32 v43, v94
	s_waitcnt lgkmcnt(2)
	v_max_f32_e64 v41, |v41|, |v41|
	v_max_f32_e32 v45, 1.0, v41
	ds_bpermute_b32 v41, v241, v121
	s_waitcnt lgkmcnt(2)
	v_max_f32_e64 v40, |v40|, |v40|
	v_max_f32_e32 v40, 1.0, v40
	s_waitcnt lgkmcnt(1)
	v_max_f32_e64 v7, |v7|, |v7|
	v_max_f32_e32 v7, 1.0, v7
	s_waitcnt lgkmcnt(0)
	v_max_f32_e64 v41, |v41|, |v41|
	v_max_f32_e32 v47, 1.0, v41
	v_div_scale_f32 v41, s[80:81], v40, v40, 1.0
	v_rcp_f32_e32 v49, v41
	v_mov_b32_e32 v94, v115
	s_waitcnt lgkmcnt(0)
	s_barrier
	v_fma_f32 v51, -v41, v49, 1.0
	v_fmac_f32_e32 v49, v51, v49
	v_div_scale_f32 v51, vcc, 1.0, v40, 1.0
	v_mul_f32_e32 v52, v51, v49
	v_fma_f32 v53, -v41, v52, v51
	v_fmac_f32_e32 v52, v53, v49
	v_fma_f32 v41, -v41, v52, v51
	v_div_fmas_f32 v41, v41, v49, v52
	v_div_fixup_f32 v53, v41, v40, 1.0
	v_div_scale_f32 v40, s[80:81], v7, v7, 1.0
	v_rcp_f32_e32 v41, v40
	s_nop 0
	v_fma_f32 v49, -v40, v41, 1.0
	v_fmac_f32_e32 v41, v49, v41
	v_div_scale_f32 v49, vcc, 1.0, v7, 1.0
	v_mul_f32_e32 v51, v49, v41
	v_fma_f32 v52, -v40, v51, v49
	v_fmac_f32_e32 v51, v52, v41
	v_fma_f32 v40, -v40, v51, v49
	v_div_fmas_f32 v40, v40, v41, v51
	v_div_fixup_f32 v52, v40, v7, 1.0
	v_div_scale_f32 v7, s[80:81], v47, v47, 1.0
	v_pk_mul_f32 v[122:123], v[74:75], v[52:53]
	v_pk_mul_f32 v[74:75], v[42:43], v[52:53] op_sel_hi:[1,0]
	v_rcp_f32_e32 v42, v7
	v_pk_mul_f32 v[128:129], v[62:63], v[52:53]
	v_pk_mul_f32 v[132:133], v[54:55], v[52:53]
	v_pk_mul_f32 v[40:41], v[128:129], v[128:129]
	v_fma_f32 v43, -v7, v42, 1.0
	v_fmac_f32_e32 v42, v43, v42
	v_div_scale_f32 v43, vcc, 1.0, v47, 1.0
	v_mul_f32_e32 v49, v43, v42
	v_fma_f32 v51, -v7, v49, v43
	v_fmac_f32_e32 v49, v51, v42
	v_fma_f32 v7, -v7, v49, v43
	v_div_fmas_f32 v7, v7, v42, v49
	v_div_fixup_f32 v143, v7, v47, 1.0
	v_div_scale_f32 v7, s[80:81], v45, v45, 1.0
	v_rcp_f32_e32 v42, v7
	v_pk_fma_f32 v[40:41], v[132:133], v[132:133], v[40:41]
	v_pk_mul_f32 v[124:125], v[58:59], v[52:53]
	v_pk_mul_f32 v[120:121], v[70:71], v[52:53]
	v_fma_f32 v43, -v7, v42, 1.0
	v_fmac_f32_e32 v42, v43, v42
	v_div_scale_f32 v43, vcc, 1.0, v45, 1.0
	v_mul_f32_e32 v47, v43, v42
	v_fma_f32 v49, -v7, v47, v43
	v_pk_fma_f32 v[40:41], v[124:125], v[124:125], v[40:41]
	v_fmac_f32_e32 v47, v49, v42
	v_pk_fma_f32 v[40:41], v[122:123], v[122:123], v[40:41]
	v_fma_f32 v7, -v7, v47, v43
	v_pk_fma_f32 v[40:41], v[120:121], v[120:121], v[40:41]
	v_pk_mul_f32 v[118:119], v[66:67], v[52:53]
	v_div_fmas_f32 v7, v7, v42, v47
	v_pk_fma_f32 v[40:41], v[118:119], v[118:119], v[40:41]
	v_pk_mul_f32 v[114:115], v[78:79], v[52:53]
	v_div_fixup_f32 v142, v7, v45, 1.0
	v_pk_fma_f32 v[54:55], v[114:115], v[114:115], v[40:41]
	v_pk_mul_f32 v[40:41], v[90:91], v[52:53]
	v_pk_mul_f32 v[130:131], v[64:65], v[142:143]
	v_pk_fma_f32 v[54:55], v[40:41], v[40:41], v[54:55]
	v_pk_mul_f32 v[86:87], v[86:87], v[52:53]
	v_pk_mul_f32 v[134:135], v[56:57], v[142:143]
	v_pk_mul_f32 v[42:43], v[130:131], v[130:131]
	v_pk_fma_f32 v[54:55], v[86:87], v[86:87], v[54:55]
	v_pk_mul_f32 v[78:79], v[82:83], v[52:53]
	v_pk_fma_f32 v[42:43], v[134:135], v[134:135], v[42:43]
	v_pk_mul_f32 v[126:127], v[60:61], v[142:143]
	v_pk_fma_f32 v[136:137], v[78:79], v[78:79], v[54:55]
	v_mov_b32_e32 v54, v53
	v_mov_b32_e32 v58, v116
	v_mov_b32_e32 v59, v96
	v_mov_b32_e32 v96, v117
	v_pk_fma_f32 v[42:43], v[126:127], v[126:127], v[42:43]
	v_pk_mul_f32 v[116:117], v[76:77], v[142:143]
	v_pk_mul_f32 v[70:71], v[94:95], v[54:55] op_sel_hi:[1,0]
	v_pk_fma_f32 v[42:43], v[116:117], v[116:117], v[42:43]
	v_pk_mul_f32 v[94:95], v[72:73], v[142:143]
	v_pk_mul_f32 v[90:91], v[68:69], v[142:143]
	v_pk_fma_f32 v[42:43], v[94:95], v[94:95], v[42:43]
	v_pk_mul_f32 v[82:83], v[80:81], v[142:143]
	v_pk_fma_f32 v[42:43], v[90:91], v[90:91], v[42:43]
	v_pk_mul_f32 v[80:81], v[88:89], v[142:143]
	v_pk_fma_f32 v[56:57], v[82:83], v[82:83], v[42:43]
	v_pk_mul_f32 v[42:43], v[92:93], v[142:143]
	v_pk_mul_f32 v[76:77], v[84:85], v[142:143]
	v_pk_fma_f32 v[56:57], v[42:43], v[42:43], v[56:57]
	v_pk_mul_f32 v[138:139], v[74:75], v[74:75]
	v_pk_fma_f32 v[56:57], v[80:81], v[80:81], v[56:57]
	v_pk_mul_f32 v[140:141], v[70:71], v[70:71]
	v_pk_fma_f32 v[88:89], v[76:77], v[76:77], v[56:57]
	v_mov_b32_e32 v56, v106
	v_mov_b32_e32 v57, v102
	v_pk_mul_f32 v[62:63], v[56:57], v[52:53] op_sel_hi:[1,0]
	v_mov_b32_e32 v56, v108
	v_mov_b32_e32 v57, v104
	v_pk_mul_f32 v[66:67], v[56:57], v[142:143] op_sel_hi:[1,0]
	v_mov_b32_e32 v56, v110
	v_mov_b32_e32 v57, v98
	v_mov_b32_e32 v84, v143
	v_mov_b32_e32 v102, v107
	v_mov_b32_e32 v104, v109
	v_pk_mul_f32 v[56:57], v[56:57], v[52:53] op_sel_hi:[1,0]
	v_mov_b32_e32 v98, v111
	v_mov_b32_e32 v52, v112
	v_mov_b32_e32 v53, v100
	v_mov_b32_e32 v100, v113
	v_pk_mul_f32 v[72:73], v[58:59], v[142:143] op_sel_hi:[1,0]
	v_pk_mul_f32 v[68:69], v[96:97], v[84:85] op_sel_hi:[1,0]
	v_pk_mul_f32 v[64:65], v[102:103], v[54:55] op_sel_hi:[1,0]
	v_pk_mul_f32 v[60:61], v[104:105], v[84:85] op_sel_hi:[1,0]
	v_pk_mul_f32 v[58:59], v[98:99], v[54:55] op_sel_hi:[1,0]
	v_pk_mul_f32 v[54:55], v[52:53], v[142:143] op_sel_hi:[1,0]
	v_pk_mul_f32 v[52:53], v[100:101], v[84:85] op_sel_hi:[1,0]
	v_mov_b32_e32 v85, v138
	v_mov_b32_e32 v138, v141
	v_pk_mul_f32 v[144:145], v[62:63], v[62:63]
	v_pk_mul_f32 v[102:103], v[64:65], v[64:65]
	v_mov_b32_e32 v84, v140
	v_pk_add_f32 v[112:113], v[138:139], v[136:137] op_sel:[0,1] op_sel_hi:[1,0]
	v_pk_mul_f32 v[108:109], v[56:57], v[56:57]
	v_pk_add_f32 v[84:85], v[84:85], v[112:113]
	v_mov_b32_e32 v112, v103
	v_mov_b32_e32 v113, v145
	v_pk_mul_f32 v[98:99], v[58:59], v[58:59]
	v_pk_add_f32 v[84:85], v[112:113], v[84:85]
	v_mov_b32_e32 v103, v144
	v_pk_add_f32 v[84:85], v[102:103], v[84:85]
	v_mov_b32_e32 v102, v99
	v_mov_b32_e32 v103, v109
	v_pk_add_f32 v[84:85], v[102:103], v[84:85]
	v_mov_b32_e32 v99, v108
	v_pk_add_f32 v[84:85], v[98:99], v[84:85]
	ds_bpermute_b32 v99, v242, v85
	ds_bpermute_b32 v98, v242, v84
	v_pk_mul_f32 v[92:93], v[72:73], v[72:73]
	v_pk_mul_f32 v[96:97], v[68:69], v[68:69]
	v_mov_b32_e32 v103, v92
	v_mov_b32_e32 v92, v97
	s_waitcnt lgkmcnt(0)
	v_pk_add_f32 v[84:85], v[84:85], v[98:99]
	ds_bpermute_b32 v99, v243, v85
	ds_bpermute_b32 v98, v243, v84
	v_pk_mul_f32 v[106:107], v[66:67], v[66:67]
	v_pk_mul_f32 v[104:105], v[60:61], v[60:61]
	v_mov_b32_e32 v102, v96
	v_pk_add_f32 v[88:89], v[92:93], v[88:89] op_sel:[0,1] op_sel_hi:[1,0]
	v_mov_b32_e32 v92, v105
	v_pk_add_f32 v[88:89], v[102:103], v[88:89]
	v_mov_b32_e32 v93, v107
	v_pk_mul_f32 v[110:111], v[54:55], v[54:55]
	v_pk_mul_f32 v[100:101], v[52:53], v[52:53]
	v_pk_add_f32 v[88:89], v[92:93], v[88:89]
	v_mov_b32_e32 v105, v106
	s_waitcnt lgkmcnt(0)
	v_pk_add_f32 v[84:85], v[84:85], v[98:99]
	v_pk_add_f32 v[88:89], v[104:105], v[88:89]
	v_mov_b32_e32 v92, v101
	v_mov_b32_e32 v93, v111
	ds_bpermute_b32 v99, v244, v85
	ds_bpermute_b32 v98, v244, v84
	v_pk_add_f32 v[88:89], v[92:93], v[88:89]
	v_mov_b32_e32 v101, v110
	v_pk_add_f32 v[88:89], v[100:101], v[88:89]
	ds_bpermute_b32 v93, v242, v89
	ds_bpermute_b32 v92, v242, v88
	s_waitcnt lgkmcnt(2)
	v_pk_add_f32 v[84:85], v[84:85], v[98:99]
	ds_bpermute_b32 v99, v245, v85
	ds_bpermute_b32 v98, v245, v84
	s_mov_b32 s80, 0x358637bd
	s_waitcnt lgkmcnt(2)
	v_pk_add_f32 v[88:89], v[88:89], v[92:93]
	ds_bpermute_b32 v93, v243, v89
	ds_bpermute_b32 v92, v243, v88
	s_waitcnt lgkmcnt(2)
	v_pk_add_f32 v[84:85], v[84:85], v[98:99]
	v_mov_b64_e32 v[98:99], s[80:81]
	v_pk_fma_f32 v[84:85], v[84:85], s[8:9], v[98:99] op_sel_hi:[1,0,0]
	s_waitcnt lgkmcnt(0)
	v_pk_add_f32 v[88:89], v[88:89], v[92:93]
	v_mul_f32_e32 v7, 0x4b800000, v85
	v_cmp_gt_f32_e64 s[80:81], s42, v85
	ds_bpermute_b32 v93, v244, v89
	ds_bpermute_b32 v92, v244, v88
	v_cndmask_b32_e64 v7, v85, v7, s[80:81]
	v_rsq_f32_e32 v7, v7
	v_cmp_gt_f32_e32 vcc, s42, v84
	s_waitcnt lgkmcnt(0)
	v_pk_add_f32 v[88:89], v[88:89], v[92:93]
	v_mul_f32_e32 v45, 0x45800000, v7
	v_cndmask_b32_e64 v7, v7, v45, s[80:81]
	v_mul_f32_e32 v45, 0x4b800000, v84
	ds_bpermute_b32 v93, v245, v89
	ds_bpermute_b32 v92, v245, v88
	v_cndmask_b32_e32 v45, v84, v45, vcc
	v_rsq_f32_e32 v45, v45
	v_mul_f32_e32 v40, v40, v7
	s_waitcnt lgkmcnt(0)
	v_pk_add_f32 v[88:89], v[88:89], v[92:93]
	v_mul_f32_e32 v47, 0x45800000, v45
	v_pk_fma_f32 v[88:89], v[88:89], s[8:9], v[98:99] op_sel_hi:[1,0,0]
	v_cndmask_b32_e32 v84, v45, v47, vcc
	v_mul_f32_e32 v45, 0x4b800000, v89
	v_cmp_gt_f32_e64 s[80:81], s42, v89
	v_cmp_gt_f32_e32 vcc, s42, v88
	s_nop 0
	v_cndmask_b32_e64 v45, v89, v45, s[80:81]
	v_rsq_f32_e32 v45, v45
	s_nop 0
	v_mul_f32_e32 v47, 0x45800000, v45
	v_cndmask_b32_e64 v85, v45, v47, s[80:81]
	v_mul_f32_e32 v45, 0x4b800000, v88
	v_cndmask_b32_e32 v45, v88, v45, vcc
	v_rsq_f32_e32 v45, v45
	s_nop 0
	v_mul_f32_e32 v47, 0x45800000, v45
	v_cndmask_b32_e32 v88, v45, v47, vcc
	v_mul_f32_e32 v47, v132, v7
	s_waitcnt vmcnt(0)
	v_mul_f32_e32 v47, v146, v47
	v_mul_f32_e32 v49, v133, v84
	v_mul_f32_e32 v49, v146, v49
	v_cvt_pk_bf16_f32 v47, v47, v49
	ds_write_b16 v238, v47
	ds_write_b16_d16_hi v238, v47 offset:272
	v_mul_f32_e32 v47, v134, v85
	v_mul_f32_e32 v47, v146, v47
	v_mul_f32_e32 v49, v135, v88
	v_mul_f32_e32 v45, v146, v49
	v_cvt_pk_bf16_f32 v47, v47, v45
	ds_write_b16 v238, v47 offset:544
	ds_write_b16_d16_hi v238, v47 offset:816
	v_mul_f32_e32 v47, v128, v7
	v_mul_f32_e32 v47, v147, v47
	v_mul_f32_e32 v49, v129, v84
	v_mul_f32_e32 v49, v147, v49
	v_cvt_pk_bf16_f32 v47, v47, v49
	ds_write_b16 v238, v47 offset:32
	ds_write_b16_d16_hi v238, v47 offset:304
	v_mul_f32_e32 v47, v130, v85
	v_mul_f32_e32 v47, v147, v47
	v_mul_f32_e32 v49, v131, v88
	v_mul_f32_e32 v45, v147, v49
	v_cvt_pk_bf16_f32 v47, v47, v45
	ds_write_b16 v238, v47 offset:576
	ds_write_b16_d16_hi v238, v47 offset:848
	v_mul_f32_e32 v47, v124, v7
	v_mul_f32_e32 v47, v148, v47
	v_mul_f32_e32 v49, v125, v84
	v_mul_f32_e32 v49, v148, v49
	v_cvt_pk_bf16_f32 v47, v47, v49
	ds_write_b16 v238, v47 offset:64
	ds_write_b16_d16_hi v238, v47 offset:336
	v_mul_f32_e32 v47, v126, v85
	v_mul_f32_e32 v47, v148, v47
	v_mul_f32_e32 v49, v127, v88
	v_mul_f32_e32 v45, v148, v49
	v_cvt_pk_bf16_f32 v47, v47, v45
	ds_write_b16 v238, v47 offset:608
	ds_write_b16_d16_hi v238, v47 offset:880
	v_mul_f32_e32 v47, v122, v7
	v_mul_f32_e32 v47, v47, v149
	v_mul_f32_e32 v49, v123, v84
	v_mul_f32_e32 v49, v49, v149
	v_cvt_pk_bf16_f32 v47, v47, v49
	ds_write_b16 v238, v47 offset:96
	ds_write_b16_d16_hi v238, v47 offset:368
	v_mul_f32_e32 v47, v116, v85
	v_mul_f32_e32 v47, v149, v47
	v_mul_f32_e32 v49, v117, v88
	v_mul_f32_e32 v45, v149, v49
	v_cvt_pk_bf16_f32 v47, v47, v45
	ds_write_b16 v238, v47 offset:640
	ds_write_b16_d16_hi v238, v47 offset:912
	global_load_dword v146, v[194:195], off offset:768
	global_load_dword v147, v[194:195], off offset:832
	global_load_dword v148, v[194:195], off offset:896
	global_load_dword v149, v[194:195], off offset:960
	v_mul_f32_e32 v47, v120, v7
	v_mul_f32_e32 v47, v47, v150
	v_mul_f32_e32 v49, v121, v84
	v_mul_f32_e32 v49, v49, v150
	v_cvt_pk_bf16_f32 v47, v47, v49
	ds_write_b16 v238, v47 offset:128
	ds_write_b16_d16_hi v238, v47 offset:400
	v_mul_f32_e32 v47, v94, v85
	v_mul_f32_e32 v47, v47, v150
	v_mul_f32_e32 v49, v95, v88
	v_mul_f32_e32 v45, v49, v150
	v_cvt_pk_bf16_f32 v47, v47, v45
	ds_write_b16 v238, v47 offset:672
	ds_write_b16_d16_hi v238, v47 offset:944
	v_mul_f32_e32 v47, v118, v7
	v_mul_f32_e32 v47, v47, v151
	v_mul_f32_e32 v49, v119, v84
	v_mul_f32_e32 v49, v49, v151
	v_cvt_pk_bf16_f32 v47, v47, v49
	ds_write_b16 v238, v47 offset:160
	ds_write_b16_d16_hi v238, v47 offset:432
	v_mul_f32_e32 v47, v90, v85
	v_mul_f32_e32 v47, v47, v151
	v_mul_f32_e32 v49, v91, v88
	v_mul_f32_e32 v45, v49, v151
	v_cvt_pk_bf16_f32 v47, v47, v45
	ds_write_b16 v238, v47 offset:704
	ds_write_b16_d16_hi v238, v47 offset:976
	v_mul_f32_e32 v47, v114, v7
	v_mul_f32_e32 v47, v47, v152
	v_mul_f32_e32 v49, v115, v84
	v_mul_f32_e32 v49, v49, v152
	v_cvt_pk_bf16_f32 v47, v47, v49
	ds_write_b16 v238, v47 offset:192
	ds_write_b16_d16_hi v238, v47 offset:464
	v_mul_f32_e32 v47, v82, v85
	v_mul_f32_e32 v47, v47, v152
	v_mul_f32_e32 v49, v83, v88
	v_mul_f32_e32 v45, v49, v152
	v_cvt_pk_bf16_f32 v47, v47, v45
	ds_write_b16 v238, v47 offset:736
	ds_write_b16_d16_hi v238, v47 offset:1008
	v_mul_f32_e32 v40, v40, v153
	v_mul_f32_e32 v47, v41, v84
	v_mul_f32_e32 v47, v47, v153
	v_cvt_pk_bf16_f32 v40, v40, v47
	ds_write_b16 v238, v40 offset:224
	ds_write_b16_d16_hi v238, v40 offset:496
	v_mul_f32_e32 v40, v42, v85
	v_mul_f32_e32 v40, v40, v153
	v_mul_f32_e32 v41, v43, v88
	v_mul_f32_e32 v41, v41, v153
	v_cvt_pk_bf16_f32 v40, v40, v41
	ds_write_b16 v238, v40 offset:768
	ds_write_b16_d16_hi v238, v40 offset:1040
	s_waitcnt vmcnt(0)
	v_ashrrev_i32_e32 v51, 31, v50
	s_and_saveexec_b64 s[80:81], s[76:77]
	s_cbranch_execz .LBB0_746
	v_lshlrev_b32_e32 v45, 16, v36
	v_mul_f32_e32 v45, 0xbfb8aa3b, v45
	v_exp_f32_e32 v82, v45
	v_lshlrev_b32_e32 v45, 16, v37
	ds_read_b128 v[40:43], v239
	v_mul_f32_e32 v45, 0xbfb8aa3b, v45
	v_exp_f32_e32 v83, v45
	v_and_b32_e32 v36, 0xffff0000, v36
	v_and_b32_e32 v37, 0xffff0000, v37
	s_waitcnt lgkmcnt(0)
	v_lshlrev_b32_e32 v47, 16, v41
	v_pk_add_f32 v[82:83], v[82:83], 1.0 op_sel_hi:[1,0]
	v_lshlrev_b32_e32 v45, 16, v40
	v_rcp_f32_e32 v89, v83
	v_mul_f32_e32 v36, 0xbfb8aa3b, v36
	v_mul_f32_e32 v37, 0xbfb8aa3b, v37
	v_exp_f32_e32 v36, v36
	v_mul_f32_e32 v47, v47, v89
	v_rcp_f32_e32 v83, v82
	v_exp_f32_e32 v37, v37
	v_and_b32_e32 v40, 0xffff0000, v40
	v_and_b32_e32 v41, 0xffff0000, v41
	v_pk_add_f32 v[36:37], v[36:37], 1.0 op_sel_hi:[1,0]
	v_mul_f32_e32 v45, v45, v83
	v_rcp_f32_e32 v82, v36
	s_nop 0
	v_mul_f32_e32 v40, v40, v82
	v_rcp_f32_e32 v49, v37
	s_nop 0
	v_mul_f32_e32 v41, v41, v49
	v_and_b32_e32 v37, 0xffff0000, v38
	v_mul_f32_e32 v37, 0xbfb8aa3b, v37
	v_lshlrev_b32_e32 v36, 16, v38
	v_exp_f32_e32 v38, v37
	v_lshlrev_b32_e32 v37, 16, v39
	v_mul_f32_e32 v36, 0xbfb8aa3b, v36
	v_mul_f32_e32 v37, 0xbfb8aa3b, v37
	v_exp_f32_e32 v36, v36
	v_exp_f32_e32 v37, v37
	v_lshlrev_b32_e32 v82, 16, v43
	v_lshlrev_b32_e32 v49, 16, v42
	v_and_b32_e32 v39, 0xffff0000, v39
	v_pk_add_f32 v[36:37], v[36:37], 1.0 op_sel_hi:[1,0]
	v_mul_f32_e32 v39, 0xbfb8aa3b, v39
	v_rcp_f32_e32 v89, v37
	v_exp_f32_e32 v39, v39
	v_and_b32_e32 v42, 0xffff0000, v42
	v_and_b32_e32 v43, 0xffff0000, v43
	v_mul_f32_e32 v82, v82, v89
	v_rcp_f32_e32 v83, v36
	s_nop 0
	v_mul_f32_e32 v49, v49, v83
	v_pk_add_f32 v[36:37], v[38:39], 1.0 op_sel_hi:[1,0]
	s_nop 0
	v_rcp_f32_e32 v39, v36
	s_nop 0
	v_mul_f32_e32 v36, v42, v39
	v_rcp_f32_e32 v39, v37
	s_nop 0
	v_mul_f32_e32 v37, v43, v39
	v_cvt_pk_bf16_f32 v39, v82, v37
	v_cvt_pk_bf16_f32 v38, v49, v36
	v_cvt_pk_bf16_f32 v37, v47, v41
	v_cvt_pk_bf16_f32 v36, v45, v40
	v_lshlrev_b64 v[40:41], 11, v[50:51]
	v_lshl_add_u64 v[40:41], v[176:177], 0, v[40:41]
	global_store_dwordx4 v[40:41], v[36:39], off sc1
	s_or_b64 exec, exec, s[80:81]
	v_ashrrev_i32_e32 v49, 31, v48
	s_and_saveexec_b64 s[80:81], s[74:75]
	s_cbranch_execnz .LBB0_747

.LBB0_745:
	v_lshlrev_b32_e32 v36, 16, v28
	v_lshlrev_b32_e32 v37, 16, v29
	ds_read_b128 v[32:35], v239 offset:2176
	v_mul_f32_e32 v36, 0xbfb8aa3b, v36
	v_mul_f32_e32 v37, 0xbfb8aa3b, v37
	v_exp_f32_e32 v36, v36
	v_exp_f32_e32 v37, v37
	s_waitcnt lgkmcnt(0)
	v_lshlrev_b32_e32 v39, 16, v33
	v_lshlrev_b32_e32 v38, 16, v32
	v_and_b32_e32 v28, 0xffff0000, v28
	v_pk_add_f32 v[36:37], v[36:37], 1.0 op_sel_hi:[1,0]
	v_and_b32_e32 v29, 0xffff0000, v29
	v_rcp_f32_e32 v41, v37
	v_mul_f32_e32 v28, 0xbfb8aa3b, v28
	v_mul_f32_e32 v29, 0xbfb8aa3b, v29
	v_exp_f32_e32 v28, v28
	v_mul_f32_e32 v37, v39, v41
	v_rcp_f32_e32 v40, v36
	v_exp_f32_e32 v29, v29
	v_and_b32_e32 v32, 0xffff0000, v32
	v_and_b32_e32 v33, 0xffff0000, v33
	v_pk_add_f32 v[28:29], v[28:29], 1.0 op_sel_hi:[1,0]
	v_mul_f32_e32 v36, v38, v40
	v_rcp_f32_e32 v39, v28
	s_nop 0
	v_mul_f32_e32 v32, v32, v39
	v_rcp_f32_e32 v38, v29
	s_nop 0
	v_mul_f32_e32 v33, v33, v38
	v_and_b32_e32 v29, 0xffff0000, v30
	v_mul_f32_e32 v29, 0xbfb8aa3b, v29
	v_lshlrev_b32_e32 v28, 16, v30
	v_exp_f32_e32 v30, v29
	v_lshlrev_b32_e32 v29, 16, v31
	v_mul_f32_e32 v28, 0xbfb8aa3b, v28
	v_mul_f32_e32 v29, 0xbfb8aa3b, v29
	v_exp_f32_e32 v28, v28
	v_exp_f32_e32 v29, v29
	v_lshlrev_b32_e32 v39, 16, v35
	v_lshlrev_b32_e32 v38, 16, v34
	v_and_b32_e32 v31, 0xffff0000, v31
	v_pk_add_f32 v[28:29], v[28:29], 1.0 op_sel_hi:[1,0]
	v_mul_f32_e32 v31, 0xbfb8aa3b, v31
	v_rcp_f32_e32 v41, v29
	v_exp_f32_e32 v31, v31
	v_and_b32_e32 v34, 0xffff0000, v34
	v_and_b32_e32 v35, 0xffff0000, v35
	v_mul_f32_e32 v39, v39, v41
	v_rcp_f32_e32 v40, v28
	s_nop 0
	v_mul_f32_e32 v38, v38, v40
	v_pk_add_f32 v[28:29], v[30:31], 1.0 op_sel_hi:[1,0]
	s_nop 0
	v_rcp_f32_e32 v31, v28
	s_nop 0
	v_mul_f32_e32 v28, v34, v31
	v_rcp_f32_e32 v31, v29
	s_nop 0
	v_mul_f32_e32 v29, v35, v31
	v_cvt_pk_bf16_f32 v31, v39, v29
	v_cvt_pk_bf16_f32 v30, v38, v28
	v_cvt_pk_bf16_f32 v29, v37, v33
	v_cvt_pk_bf16_f32 v28, v36, v32
	v_lshlrev_b64 v[32:33], 11, v[46:47]
	v_lshl_add_u64 v[32:33], v[176:177], 0, v[32:33]
	global_store_dwordx4 v[32:33], v[28:31], off sc1
	s_or_b64 exec, exec, s[80:81]
	v_ashrrev_i32_e32 v45, 31, v44
	s_and_saveexec_b64 s[80:81], s[70:71]
	s_cbranch_execnz .LBB0_749
	s_branch .LBB0_750

.LBB0_747:
	v_lshlrev_b32_e32 v40, 16, v32
	v_lshlrev_b32_e32 v41, 16, v33
	ds_read_b128 v[36:39], v239 offset:1088
	v_mul_f32_e32 v40, 0xbfb8aa3b, v40
	v_mul_f32_e32 v41, 0xbfb8aa3b, v41
	v_exp_f32_e32 v40, v40
	v_exp_f32_e32 v41, v41
	s_waitcnt lgkmcnt(0)
	v_lshlrev_b32_e32 v43, 16, v37
	v_lshlrev_b32_e32 v42, 16, v36
	v_and_b32_e32 v32, 0xffff0000, v32
	v_pk_add_f32 v[40:41], v[40:41], 1.0 op_sel_hi:[1,0]
	v_and_b32_e32 v33, 0xffff0000, v33
	v_rcp_f32_e32 v47, v41
	v_mul_f32_e32 v32, 0xbfb8aa3b, v32
	v_mul_f32_e32 v33, 0xbfb8aa3b, v33
	v_exp_f32_e32 v32, v32
	v_mul_f32_e32 v41, v43, v47
	v_rcp_f32_e32 v45, v40
	v_exp_f32_e32 v33, v33
	v_and_b32_e32 v36, 0xffff0000, v36
	v_and_b32_e32 v37, 0xffff0000, v37
	v_pk_add_f32 v[32:33], v[32:33], 1.0 op_sel_hi:[1,0]
	v_mul_f32_e32 v40, v42, v45
	v_rcp_f32_e32 v43, v32
	s_nop 0
	v_mul_f32_e32 v36, v36, v43
	v_rcp_f32_e32 v42, v33
	s_nop 0
	v_mul_f32_e32 v37, v37, v42
	v_and_b32_e32 v33, 0xffff0000, v34
	v_mul_f32_e32 v33, 0xbfb8aa3b, v33
	v_lshlrev_b32_e32 v32, 16, v34
	v_exp_f32_e32 v34, v33
	v_lshlrev_b32_e32 v33, 16, v35
	v_mul_f32_e32 v32, 0xbfb8aa3b, v32
	v_mul_f32_e32 v33, 0xbfb8aa3b, v33
	v_exp_f32_e32 v32, v32
	v_exp_f32_e32 v33, v33
	v_lshlrev_b32_e32 v43, 16, v39
	v_lshlrev_b32_e32 v42, 16, v38
	v_and_b32_e32 v35, 0xffff0000, v35
	v_pk_add_f32 v[32:33], v[32:33], 1.0 op_sel_hi:[1,0]
	v_mul_f32_e32 v35, 0xbfb8aa3b, v35
	v_rcp_f32_e32 v47, v33
	v_exp_f32_e32 v35, v35
	v_and_b32_e32 v38, 0xffff0000, v38
	v_and_b32_e32 v39, 0xffff0000, v39
	v_mul_f32_e32 v43, v43, v47
	v_rcp_f32_e32 v45, v32
	s_nop 0
	v_mul_f32_e32 v42, v42, v45
	v_pk_add_f32 v[32:33], v[34:35], 1.0 op_sel_hi:[1,0]
	s_nop 0
	v_rcp_f32_e32 v35, v32
	s_nop 0
	v_mul_f32_e32 v32, v38, v35
	v_rcp_f32_e32 v35, v33
	s_nop 0
	v_mul_f32_e32 v33, v39, v35
	v_cvt_pk_bf16_f32 v35, v43, v33
	v_cvt_pk_bf16_f32 v34, v42, v32
	v_cvt_pk_bf16_f32 v33, v41, v37
	v_cvt_pk_bf16_f32 v32, v40, v36
	v_lshlrev_b64 v[36:37], 11, v[48:49]
	v_lshl_add_u64 v[36:37], v[176:177], 0, v[36:37]
	global_store_dwordx4 v[36:37], v[32:35], off sc1
	s_or_b64 exec, exec, s[80:81]
	v_ashrrev_i32_e32 v47, 31, v46
	s_and_saveexec_b64 s[80:81], s[72:73]
	s_cbranch_execnz .LBB0_745

.LBB0_749:
	v_lshlrev_b32_e32 v32, 16, v24
	v_lshlrev_b32_e32 v33, 16, v25
	ds_read_b128 v[28:31], v239 offset:3264
	v_mul_f32_e32 v32, 0xbfb8aa3b, v32
	v_mul_f32_e32 v33, 0xbfb8aa3b, v33
	v_exp_f32_e32 v32, v32
	v_exp_f32_e32 v33, v33
	s_waitcnt lgkmcnt(0)
	v_lshlrev_b32_e32 v35, 16, v29
	v_lshlrev_b32_e32 v34, 16, v28
	v_and_b32_e32 v24, 0xffff0000, v24
	v_pk_add_f32 v[32:33], v[32:33], 1.0 op_sel_hi:[1,0]
	v_and_b32_e32 v25, 0xffff0000, v25
	v_rcp_f32_e32 v37, v33
	v_mul_f32_e32 v24, 0xbfb8aa3b, v24
	v_mul_f32_e32 v25, 0xbfb8aa3b, v25
	v_exp_f32_e32 v24, v24
	v_mul_f32_e32 v33, v35, v37
	v_rcp_f32_e32 v36, v32
	v_exp_f32_e32 v25, v25
	v_and_b32_e32 v28, 0xffff0000, v28
	v_and_b32_e32 v29, 0xffff0000, v29
	v_pk_add_f32 v[24:25], v[24:25], 1.0 op_sel_hi:[1,0]
	v_mul_f32_e32 v32, v34, v36
	v_rcp_f32_e32 v35, v24
	s_nop 0
	v_mul_f32_e32 v28, v28, v35
	v_rcp_f32_e32 v34, v25
	s_nop 0
	v_mul_f32_e32 v29, v29, v34
	v_and_b32_e32 v25, 0xffff0000, v26
	v_mul_f32_e32 v25, 0xbfb8aa3b, v25
	v_lshlrev_b32_e32 v24, 16, v26
	v_exp_f32_e32 v26, v25
	v_lshlrev_b32_e32 v25, 16, v27
	v_mul_f32_e32 v24, 0xbfb8aa3b, v24
	v_mul_f32_e32 v25, 0xbfb8aa3b, v25
	v_exp_f32_e32 v24, v24
	v_exp_f32_e32 v25, v25
	v_lshlrev_b32_e32 v35, 16, v31
	v_lshlrev_b32_e32 v34, 16, v30
	v_and_b32_e32 v27, 0xffff0000, v27
	v_pk_add_f32 v[24:25], v[24:25], 1.0 op_sel_hi:[1,0]
	v_mul_f32_e32 v27, 0xbfb8aa3b, v27
	v_rcp_f32_e32 v37, v25
	v_exp_f32_e32 v27, v27
	v_and_b32_e32 v30, 0xffff0000, v30
	v_and_b32_e32 v31, 0xffff0000, v31
	v_mul_f32_e32 v35, v35, v37
	v_rcp_f32_e32 v36, v24
	s_nop 0
	v_mul_f32_e32 v34, v34, v36
	v_pk_add_f32 v[24:25], v[26:27], 1.0 op_sel_hi:[1,0]
	s_nop 0
	v_rcp_f32_e32 v27, v24
	s_nop 0
	v_mul_f32_e32 v24, v30, v27
	v_rcp_f32_e32 v27, v25
	s_nop 0
	v_mul_f32_e32 v25, v31, v27
	v_cvt_pk_bf16_f32 v27, v35, v25
	v_cvt_pk_bf16_f32 v26, v34, v24
	v_cvt_pk_bf16_f32 v25, v33, v29
	v_cvt_pk_bf16_f32 v24, v32, v28
	v_lshlrev_b64 v[28:29], 11, v[44:45]
	v_lshl_add_u64 v[28:29], v[176:177], 0, v[28:29]
	global_store_dwordx4 v[28:29], v[24:27], off sc1
.LBB0_750:
	s_or_b64 exec, exec, s[80:81]
	s_nop 1
	v_mul_f32_e32 v25, v86, v7
	v_mul_f32_e32 v25, v25, v154
	v_mul_f32_e32 v26, v87, v84
	v_mul_f32_e32 v26, v26, v154
	v_cvt_pk_bf16_f32 v25, v25, v26
	ds_write_b16 v238, v25
	ds_write_b16_d16_hi v238, v25 offset:272
	v_mul_f32_e32 v25, v80, v85
	v_mul_f32_e32 v25, v25, v154
	v_mul_f32_e32 v26, v81, v88
	v_mul_f32_e32 v24, v26, v154
	v_cvt_pk_bf16_f32 v25, v25, v24
	ds_write_b16 v238, v25 offset:544
	ds_write_b16_d16_hi v238, v25 offset:816
	v_mul_f32_e32 v25, v78, v7
	v_mul_f32_e32 v25, v25, v155
	v_mul_f32_e32 v26, v79, v84
	v_mul_f32_e32 v26, v26, v155
	v_cvt_pk_bf16_f32 v25, v25, v26
	ds_write_b16 v238, v25 offset:32
	ds_write_b16_d16_hi v238, v25 offset:304
	v_mul_f32_e32 v25, v76, v85
	v_mul_f32_e32 v25, v25, v155
	v_mul_f32_e32 v26, v77, v88
	v_mul_f32_e32 v24, v26, v155
	v_cvt_pk_bf16_f32 v25, v25, v24
	ds_write_b16 v238, v25 offset:576
	ds_write_b16_d16_hi v238, v25 offset:848
	v_mul_f32_e32 v25, v75, v7
	v_mul_f32_e32 v25, v25, v156
	v_mul_f32_e32 v26, v71, v84
	v_mul_f32_e32 v26, v26, v156
	v_cvt_pk_bf16_f32 v25, v25, v26
	ds_write_b16 v238, v25 offset:64
	ds_write_b16_d16_hi v238, v25 offset:336
	v_mul_f32_e32 v25, v73, v85
	v_mul_f32_e32 v25, v25, v156
	v_mul_f32_e32 v26, v69, v88
	v_mul_f32_e32 v24, v26, v156
	v_cvt_pk_bf16_f32 v25, v25, v24
	ds_write_b16 v238, v25 offset:608
	ds_write_b16_d16_hi v238, v25 offset:880
	v_mul_f32_e32 v25, v74, v7
	v_mul_f32_e32 v25, v25, v157
	v_mul_f32_e32 v26, v70, v84
	v_mul_f32_e32 v26, v26, v157
	v_cvt_pk_bf16_f32 v25, v25, v26
	ds_write_b16 v238, v25 offset:96
	ds_write_b16_d16_hi v238, v25 offset:368
	v_mul_f32_e32 v25, v72, v85
	v_mul_f32_e32 v25, v25, v157
	v_mul_f32_e32 v26, v68, v88
	v_mul_f32_e32 v24, v26, v157
	v_cvt_pk_bf16_f32 v25, v25, v24
	ds_write_b16 v238, v25 offset:640
	ds_write_b16_d16_hi v238, v25 offset:912
	v_mul_f32_e32 v25, v63, v7
	v_mul_f32_e32 v25, v25, v146
	v_mul_f32_e32 v26, v65, v84
	v_mul_f32_e32 v26, v26, v146
	v_cvt_pk_bf16_f32 v25, v25, v26
	ds_write_b16 v238, v25 offset:128
	ds_write_b16_d16_hi v238, v25 offset:400
	v_mul_f32_e32 v25, v67, v85
	v_mul_f32_e32 v25, v25, v146
	v_mul_f32_e32 v26, v61, v88
	v_mul_f32_e32 v24, v26, v146
	v_cvt_pk_bf16_f32 v25, v25, v24
	ds_write_b16 v238, v25 offset:672
	ds_write_b16_d16_hi v238, v25 offset:944
	v_mul_f32_e32 v25, v62, v7
	v_mul_f32_e32 v25, v25, v147
	v_mul_f32_e32 v26, v64, v84
	v_mul_f32_e32 v26, v26, v147
	v_cvt_pk_bf16_f32 v25, v25, v26
	ds_write_b16 v238, v25 offset:160
	ds_write_b16_d16_hi v238, v25 offset:432
	v_mul_f32_e32 v25, v66, v85
	v_mul_f32_e32 v25, v25, v147
	v_mul_f32_e32 v26, v60, v88
	v_mul_f32_e32 v24, v26, v147
	v_cvt_pk_bf16_f32 v25, v25, v24
	ds_write_b16 v238, v25 offset:704
	ds_write_b16_d16_hi v238, v25 offset:976
	v_mul_f32_e32 v25, v57, v7
	v_mul_f32_e32 v7, v56, v7
	v_mul_f32_e32 v25, v25, v148
	v_mul_f32_e32 v26, v59, v84
	v_mul_f32_e32 v26, v26, v148
	v_cvt_pk_bf16_f32 v25, v25, v26
	ds_write_b16 v238, v25 offset:192
	ds_write_b16_d16_hi v238, v25 offset:464
	v_mul_f32_e32 v25, v55, v85
	v_mul_f32_e32 v25, v25, v148
	v_mul_f32_e32 v26, v53, v88
	v_mul_f32_e32 v24, v26, v148
	v_cvt_pk_bf16_f32 v25, v25, v24
	ds_write_b16 v238, v25 offset:736
	ds_write_b16_d16_hi v238, v25 offset:1008
	v_mul_f32_e32 v7, v7, v149
	v_mul_f32_e32 v25, v58, v84
	v_mul_f32_e32 v25, v25, v149
	v_cvt_pk_bf16_f32 v7, v7, v25
	ds_write_b16 v238, v7 offset:224
	ds_write_b16_d16_hi v238, v7 offset:496
	v_mul_f32_e32 v7, v54, v85
	v_mul_f32_e32 v7, v7, v149
	v_mul_f32_e32 v25, v52, v88
	v_mul_f32_e32 v25, v25, v149
	v_cvt_pk_bf16_f32 v7, v7, v25
	ds_write_b16 v238, v7 offset:768
	ds_write_b16_d16_hi v238, v7 offset:1040
	s_and_saveexec_b64 s[80:81], s[76:77]
	s_cbranch_execz .LBB0_754
	v_lshlrev_b32_e32 v7, 16, v20
	v_mul_f32_e32 v7, 0xbfb8aa3b, v7
	v_exp_f32_e32 v28, v7
	v_and_b32_e32 v7, 0xffff0000, v20
	v_mul_f32_e32 v7, 0xbfb8aa3b, v7
	v_exp_f32_e32 v20, v7
	v_lshlrev_b32_e32 v7, 16, v21
	ds_read_b128 v[24:27], v239
	v_mul_f32_e32 v7, 0xbfb8aa3b, v7
	v_exp_f32_e32 v29, v7
	v_and_b32_e32 v7, 0xffff0000, v21
	v_mul_f32_e32 v7, 0xbfb8aa3b, v7
	s_waitcnt lgkmcnt(0)
	v_lshlrev_b32_e32 v30, 16, v25
	v_pk_add_f32 v[28:29], v[28:29], 1.0 op_sel_hi:[1,0]
	v_exp_f32_e32 v21, v7
	v_rcp_f32_e32 v32, v29
	v_lshlrev_b32_e32 v7, 16, v24
	v_and_b32_e32 v24, 0xffff0000, v24
	v_pk_add_f32 v[20:21], v[20:21], 1.0 op_sel_hi:[1,0]
	v_mul_f32_e32 v29, v30, v32
	v_rcp_f32_e32 v31, v28
	v_and_b32_e32 v25, 0xffff0000, v25
	v_mul_f32_e32 v7, v7, v31
	v_rcp_f32_e32 v30, v20
	s_nop 0
	v_mul_f32_e32 v24, v24, v30
	v_rcp_f32_e32 v28, v21
	s_nop 0
	v_mul_f32_e32 v25, v25, v28
	v_and_b32_e32 v21, 0xffff0000, v22
	v_mul_f32_e32 v21, 0xbfb8aa3b, v21
	v_lshlrev_b32_e32 v20, 16, v22
	v_exp_f32_e32 v22, v21
	v_lshlrev_b32_e32 v21, 16, v23
	v_mul_f32_e32 v20, 0xbfb8aa3b, v20
	v_mul_f32_e32 v21, 0xbfb8aa3b, v21
	v_exp_f32_e32 v20, v20
	v_exp_f32_e32 v21, v21
	v_lshlrev_b32_e32 v30, 16, v27
	v_lshlrev_b32_e32 v28, 16, v26
	v_and_b32_e32 v23, 0xffff0000, v23
	v_pk_add_f32 v[20:21], v[20:21], 1.0 op_sel_hi:[1,0]
	v_mul_f32_e32 v23, 0xbfb8aa3b, v23
	v_rcp_f32_e32 v32, v21
	v_exp_f32_e32 v23, v23
	v_and_b32_e32 v26, 0xffff0000, v26
	v_and_b32_e32 v27, 0xffff0000, v27
	v_mul_f32_e32 v30, v30, v32
	v_rcp_f32_e32 v31, v20
	s_nop 0
	v_mul_f32_e32 v28, v28, v31
	v_pk_add_f32 v[20:21], v[22:23], 1.0 op_sel_hi:[1,0]
	s_nop 0
	v_rcp_f32_e32 v23, v20
	s_nop 0
	v_mul_f32_e32 v20, v26, v23
	v_rcp_f32_e32 v23, v21
	s_nop 0
	v_mul_f32_e32 v21, v27, v23
	v_cvt_pk_bf16_f32 v23, v30, v21
	v_cvt_pk_bf16_f32 v22, v28, v20
	v_cvt_pk_bf16_f32 v21, v29, v25
	v_cvt_pk_bf16_f32 v20, v7, v24
	v_lshlrev_b64 v[24:25], 11, v[50:51]
	v_lshl_add_u64 v[24:25], v[176:177], 0, v[24:25]
	global_store_dwordx4 v[24:25], v[20:23], off offset:256 sc1
	s_or_b64 exec, exec, s[80:81]
	s_and_saveexec_b64 s[76:77], s[74:75]
	s_cbranch_execnz .LBB0_755

.LBB0_753:
	v_lshlrev_b32_e32 v7, 16, v12
	v_mul_f32_e32 v7, 0xbfb8aa3b, v7
	v_exp_f32_e32 v20, v7
	v_and_b32_e32 v7, 0xffff0000, v12
	v_mul_f32_e32 v7, 0xbfb8aa3b, v7
	v_exp_f32_e32 v12, v7
	v_lshlrev_b32_e32 v7, 16, v13
	ds_read_b128 v[16:19], v239 offset:2176
	v_mul_f32_e32 v7, 0xbfb8aa3b, v7
	v_exp_f32_e32 v21, v7
	v_and_b32_e32 v7, 0xffff0000, v13
	v_mul_f32_e32 v7, 0xbfb8aa3b, v7
	s_waitcnt lgkmcnt(0)
	v_lshlrev_b32_e32 v22, 16, v17
	v_pk_add_f32 v[20:21], v[20:21], 1.0 op_sel_hi:[1,0]
	v_exp_f32_e32 v13, v7
	v_rcp_f32_e32 v24, v21
	v_lshlrev_b32_e32 v7, 16, v16
	v_and_b32_e32 v16, 0xffff0000, v16
	v_pk_add_f32 v[12:13], v[12:13], 1.0 op_sel_hi:[1,0]
	v_mul_f32_e32 v21, v22, v24
	v_rcp_f32_e32 v23, v20
	v_and_b32_e32 v17, 0xffff0000, v17
	v_mul_f32_e32 v7, v7, v23
	v_rcp_f32_e32 v22, v12
	s_nop 0
	v_mul_f32_e32 v16, v16, v22
	v_rcp_f32_e32 v20, v13
	s_nop 0
	v_mul_f32_e32 v17, v17, v20
	v_and_b32_e32 v13, 0xffff0000, v14
	v_mul_f32_e32 v13, 0xbfb8aa3b, v13
	v_lshlrev_b32_e32 v12, 16, v14
	v_exp_f32_e32 v14, v13
	v_lshlrev_b32_e32 v13, 16, v15
	v_mul_f32_e32 v12, 0xbfb8aa3b, v12
	v_mul_f32_e32 v13, 0xbfb8aa3b, v13
	v_exp_f32_e32 v12, v12
	v_exp_f32_e32 v13, v13
	v_lshlrev_b32_e32 v22, 16, v19
	v_lshlrev_b32_e32 v20, 16, v18
	v_and_b32_e32 v15, 0xffff0000, v15
	v_pk_add_f32 v[12:13], v[12:13], 1.0 op_sel_hi:[1,0]
	v_mul_f32_e32 v15, 0xbfb8aa3b, v15
	v_rcp_f32_e32 v24, v13
	v_exp_f32_e32 v15, v15
	v_and_b32_e32 v18, 0xffff0000, v18
	v_and_b32_e32 v19, 0xffff0000, v19
	v_mul_f32_e32 v22, v22, v24
	v_rcp_f32_e32 v23, v12
	s_nop 0
	v_mul_f32_e32 v20, v20, v23
	v_pk_add_f32 v[12:13], v[14:15], 1.0 op_sel_hi:[1,0]
	s_nop 0
	v_rcp_f32_e32 v15, v12
	s_nop 0
	v_mul_f32_e32 v12, v18, v15
	v_rcp_f32_e32 v15, v13
	s_nop 0
	v_mul_f32_e32 v13, v19, v15
	v_cvt_pk_bf16_f32 v15, v22, v13
	v_cvt_pk_bf16_f32 v14, v20, v12
	v_cvt_pk_bf16_f32 v13, v21, v17
	v_cvt_pk_bf16_f32 v12, v7, v16
	v_lshlrev_b64 v[16:17], 11, v[46:47]
	v_lshl_add_u64 v[16:17], v[176:177], 0, v[16:17]
	global_store_dwordx4 v[16:17], v[12:15], off offset:256 sc1
	s_or_b64 exec, exec, s[74:75]
	s_and_saveexec_b64 s[72:73], s[70:71]
	s_cbranch_execz .LBB0_688
	s_branch .LBB0_757

.LBB0_755:
	v_lshlrev_b32_e32 v7, 16, v16
	v_mul_f32_e32 v7, 0xbfb8aa3b, v7
	v_exp_f32_e32 v24, v7
	v_and_b32_e32 v7, 0xffff0000, v16
	v_mul_f32_e32 v7, 0xbfb8aa3b, v7
	v_exp_f32_e32 v16, v7
	v_lshlrev_b32_e32 v7, 16, v17
	ds_read_b128 v[20:23], v239 offset:1088
	v_mul_f32_e32 v7, 0xbfb8aa3b, v7
	v_exp_f32_e32 v25, v7
	v_and_b32_e32 v7, 0xffff0000, v17
	v_mul_f32_e32 v7, 0xbfb8aa3b, v7
	s_waitcnt lgkmcnt(0)
	v_lshlrev_b32_e32 v26, 16, v21
	v_pk_add_f32 v[24:25], v[24:25], 1.0 op_sel_hi:[1,0]
	v_exp_f32_e32 v17, v7
	v_rcp_f32_e32 v28, v25
	v_lshlrev_b32_e32 v7, 16, v20
	v_and_b32_e32 v20, 0xffff0000, v20
	v_pk_add_f32 v[16:17], v[16:17], 1.0 op_sel_hi:[1,0]
	v_mul_f32_e32 v25, v26, v28
	v_rcp_f32_e32 v27, v24
	v_and_b32_e32 v21, 0xffff0000, v21
	v_mul_f32_e32 v7, v7, v27
	v_rcp_f32_e32 v26, v16
	s_nop 0
	v_mul_f32_e32 v20, v20, v26
	v_rcp_f32_e32 v24, v17
	s_nop 0
	v_mul_f32_e32 v21, v21, v24
	v_and_b32_e32 v17, 0xffff0000, v18
	v_mul_f32_e32 v17, 0xbfb8aa3b, v17
	v_lshlrev_b32_e32 v16, 16, v18
	v_exp_f32_e32 v18, v17
	v_lshlrev_b32_e32 v17, 16, v19
	v_mul_f32_e32 v16, 0xbfb8aa3b, v16
	v_mul_f32_e32 v17, 0xbfb8aa3b, v17
	v_exp_f32_e32 v16, v16
	v_exp_f32_e32 v17, v17
	v_lshlrev_b32_e32 v26, 16, v23
	v_lshlrev_b32_e32 v24, 16, v22
	v_and_b32_e32 v19, 0xffff0000, v19
	v_pk_add_f32 v[16:17], v[16:17], 1.0 op_sel_hi:[1,0]
	v_mul_f32_e32 v19, 0xbfb8aa3b, v19
	v_rcp_f32_e32 v28, v17
	v_exp_f32_e32 v19, v19
	v_and_b32_e32 v22, 0xffff0000, v22
	v_and_b32_e32 v23, 0xffff0000, v23
	v_mul_f32_e32 v26, v26, v28
	v_rcp_f32_e32 v27, v16
	s_nop 0
	v_mul_f32_e32 v24, v24, v27
	v_pk_add_f32 v[16:17], v[18:19], 1.0 op_sel_hi:[1,0]
	s_nop 0
	v_rcp_f32_e32 v19, v16
	s_nop 0
	v_mul_f32_e32 v16, v22, v19
	v_rcp_f32_e32 v19, v17
	s_nop 0
	v_mul_f32_e32 v17, v23, v19
	v_cvt_pk_bf16_f32 v19, v26, v17
	v_cvt_pk_bf16_f32 v18, v24, v16
	v_cvt_pk_bf16_f32 v17, v25, v21
	v_cvt_pk_bf16_f32 v16, v7, v20
	v_lshlrev_b64 v[20:21], 11, v[48:49]
	v_lshl_add_u64 v[20:21], v[176:177], 0, v[20:21]
	global_store_dwordx4 v[20:21], v[16:19], off offset:256 sc1
	s_or_b64 exec, exec, s[76:77]
	s_and_saveexec_b64 s[74:75], s[72:73]
	s_cbranch_execnz .LBB0_753

.LBB0_757:
	v_lshlrev_b32_e32 v7, 16, v8
	v_mul_f32_e32 v7, 0xbfb8aa3b, v7
	v_exp_f32_e32 v16, v7
	v_and_b32_e32 v7, 0xffff0000, v8
	v_mul_f32_e32 v7, 0xbfb8aa3b, v7
	v_exp_f32_e32 v8, v7
	v_lshlrev_b32_e32 v7, 16, v9
	ds_read_b128 v[12:15], v239 offset:3264
	v_mul_f32_e32 v7, 0xbfb8aa3b, v7
	v_exp_f32_e32 v17, v7
	v_and_b32_e32 v7, 0xffff0000, v9
	v_mul_f32_e32 v7, 0xbfb8aa3b, v7
	s_waitcnt lgkmcnt(0)
	v_lshlrev_b32_e32 v18, 16, v13
	v_pk_add_f32 v[16:17], v[16:17], 1.0 op_sel_hi:[1,0]
	v_exp_f32_e32 v9, v7
	v_rcp_f32_e32 v20, v17
	v_lshlrev_b32_e32 v7, 16, v12
	v_and_b32_e32 v12, 0xffff0000, v12
	v_pk_add_f32 v[8:9], v[8:9], 1.0 op_sel_hi:[1,0]
	v_mul_f32_e32 v17, v18, v20
	v_rcp_f32_e32 v19, v16
	v_and_b32_e32 v13, 0xffff0000, v13
	v_mul_f32_e32 v7, v7, v19
	v_rcp_f32_e32 v18, v8
	s_nop 0
	v_mul_f32_e32 v12, v12, v18
	v_rcp_f32_e32 v16, v9
	s_nop 0
	v_mul_f32_e32 v13, v13, v16
	v_and_b32_e32 v9, 0xffff0000, v10
	v_mul_f32_e32 v9, 0xbfb8aa3b, v9
	v_lshlrev_b32_e32 v8, 16, v10
	v_exp_f32_e32 v10, v9
	v_lshlrev_b32_e32 v9, 16, v11
	v_mul_f32_e32 v8, 0xbfb8aa3b, v8
	v_mul_f32_e32 v9, 0xbfb8aa3b, v9
	v_exp_f32_e32 v8, v8
	v_exp_f32_e32 v9, v9
	v_lshlrev_b32_e32 v18, 16, v15
	v_lshlrev_b32_e32 v16, 16, v14
	v_and_b32_e32 v11, 0xffff0000, v11
	v_pk_add_f32 v[8:9], v[8:9], 1.0 op_sel_hi:[1,0]
	v_mul_f32_e32 v11, 0xbfb8aa3b, v11
	v_rcp_f32_e32 v20, v9
	v_exp_f32_e32 v11, v11
	v_and_b32_e32 v14, 0xffff0000, v14
	v_and_b32_e32 v15, 0xffff0000, v15
	v_mul_f32_e32 v18, v18, v20
	v_rcp_f32_e32 v19, v8
	s_nop 0
	v_mul_f32_e32 v16, v16, v19
	v_pk_add_f32 v[8:9], v[10:11], 1.0 op_sel_hi:[1,0]
	s_nop 0
	v_rcp_f32_e32 v11, v8
	s_nop 0
	v_mul_f32_e32 v8, v14, v11
	v_rcp_f32_e32 v11, v9
	s_nop 0
	v_mul_f32_e32 v9, v15, v11
	v_cvt_pk_bf16_f32 v11, v18, v9
	v_cvt_pk_bf16_f32 v10, v16, v8
	v_cvt_pk_bf16_f32 v9, v17, v13
	v_cvt_pk_bf16_f32 v8, v7, v12
	v_lshlrev_b64 v[12:13], 11, v[44:45]
	v_lshl_add_u64 v[12:13], v[176:177], 0, v[12:13]
	global_store_dwordx4 v[12:13], v[8:11], off offset:256 sc1
	s_branch .LBB0_688
